# speedup vs baseline: 1.0065x; 1.0065x over previous
.LBB1_13:
	v_mfma_f32_32x32x16_bf16 v[2:17], v[78:81], v[206:209], v[236:251]
	ds_read_b128 v[174:177], v210
	v_add_u32_e32 v195, v230, v228
	v_mfma_f32_32x32x16_bf16 v[2:17], v[74:77], v[190:193], v[2:17]
	ds_read_b128 v[170:173], v210 offset:1024
	v_exp_f32_e32 v199, v28
	v_exp_f32_e32 v198, v32
	v_exp_f32_e32 v197, v20
	v_exp_f32_e32 v196, v24
	v_mfma_f32_32x32x16_bf16 v[2:17], v[70:73], v[158:161], v[2:17]
	ds_read_b128 v[166:169], v210 offset:2048
	v_exp_f32_e32 v18, v18
	v_exp_f32_e32 v22, v22
	v_exp_f32_e32 v24, v26
	v_exp_f32_e32 v26, v30
	v_fma_f32 v20, v197, s12, s12
	v_fma_f32 v28, v196, s12, s12
	v_fma_f32 v30, v199, s12, s12
	v_fma_f32 v32, v198, s12, s12
	v_mfma_f32_32x32x16_bf16 v[2:17], v[66:69], v[142:145], v[2:17]
	ds_read_b128 v[162:165], v210 offset:3072
	v_exp_f32_e32 v19, v19
	v_exp_f32_e32 v23, v23
	v_exp_f32_e32 v27, v27
	v_exp_f32_e32 v31, v31
	v_fmac_f32_e32 v20, v18, v20
	v_fmac_f32_e32 v28, v22, v28
	v_fmac_f32_e32 v30, v24, v30
	v_fmac_f32_e32 v32, v26, v32
	v_mfma_f32_32x32x16_bf16 v[2:17], v[62:65], v[154:157], v[2:17]
	ds_read_b128 v[158:161], v210 offset:4096
	v_add_f32_e32 v22, 1.0, v19
	v_rcp_f32_e32 v19, v20
	v_rcp_f32_e32 v18, v28
	v_add_f32_e32 v20, 1.0, v23
	v_rcp_f32_e32 v191, v30
	v_rcp_f32_e32 v190, v32
	v_mfma_f32_32x32x16_bf16 v[2:17], v[58:61], v[182:185], v[2:17]
	ds_read_b128 v[154:157], v210 offset:5120
	v_exp_f32_e32 v206, v21
	v_exp_f32_e32 v207, v25
	v_add_f32_e32 v23, 1.0, v27
	v_rcp_f32_e32 v192, v20
	v_add_f32_e32 v20, 1.0, v31
	v_rcp_f32_e32 v193, v22
	v_mfma_f32_32x32x16_bf16 v[2:17], v[54:57], v[186:189], v[2:17]
	ds_read_b128 v[142:145], v210 offset:6144
	v_exp_f32_e32 v208, v29
	v_exp_f32_e32 v209, v33
	v_rcp_f32_e32 v183, v23
	v_rcp_f32_e32 v182, v20
	v_mfma_f32_32x32x16_bf16 v[2:17], v[50:53], v[134:137], v[2:17]
	ds_read_b128 v[130:133], v210 offset:7168
	v_fma_f32 v186, -v196, v18, v18
	v_fma_f32 v187, -v197, v19, v19
	ds_read_b128 v[18:21], v231 offset:36928
	ds_read_b128 v[22:25], v231 offset:36944
	ds_read_b128 v[26:29], v231 offset:36960
	ds_read_b128 v[30:33], v231 offset:36976
	v_pk_fma_f32 v[200:201], v[192:193], v[220:221], v[186:187]
	v_pk_fma_f32 v[134:135], v[198:199], v[190:191], v[190:191] neg_lo:[1,0,0] neg_hi:[1,0,0]
	s_nop 0
	v_pk_fma_f32 v[198:199], v[182:183], v[222:223], v[134:135]
	v_mfma_f32_32x32x16_bf16 v[2:17], v[46:49], v[138:141], v[2:17]
	ds_read_b128 v[134:137], v195 offset:16384
	v_add_f32_e32 v182, 1.0, v206
	v_exp_f32_e32 v183, v201
	v_exp_f32_e32 v186, v200
	v_exp_f32_e32 v187, v199
	v_exp_f32_e32 v188, v198
	v_add_f32_e32 v189, 1.0, v207
	v_add_f32_e32 v190, 1.0, v208
	v_add_f32_e32 v191, 1.0, v209
	v_mfma_f32_32x32x16_bf16 v[2:17], v[42:45], v[146:149], v[2:17]
	ds_read_b128 v[138:141], v195 offset:16416
	v_fmac_f32_e32 v182, v182, v183
	v_fmac_f32_e32 v189, v189, v186
	v_fmac_f32_e32 v190, v190, v187
	v_fmac_f32_e32 v191, v191, v188
	v_mfma_f32_32x32x16_bf16 v[2:17], v[38:41], v[150:153], v[2:17]
	ds_read_b128 v[146:149], v195 offset:16448
	v_rcp_f32_e32 v182, v182
	v_rcp_f32_e32 v189, v189
	v_mfma_f32_32x32x16_bf16 v[2:17], v[34:37], v[178:181], v[2:17]
	ds_read_b128 v[150:153], v195 offset:16480
	v_rcp_f32_e32 v190, v190
	v_rcp_f32_e32 v191, v191
	v_fma_f32 v182, -v183, v182, v182
	v_fma_f32 v183, -v186, v189, v189
	s_waitcnt lgkmcnt(4)
	v_mfma_f32_32x32x16_bf16 v[18:33], v[126:129], v[174:177], v[18:33]
	v_fma_f32 v186, -v187, v190, v190
	v_fma_f32 v187, -v188, v191, v191
	v_cvt_pk_bf16_f32 v252, v182, v183
	v_cvt_pk_bf16_f32 v253, v186, v187
	v_mfma_f32_32x32x16_bf16 v[18:33], v[122:125], v[170:173], v[18:33]
	s_nop 1
	v_exp_f32_e32 v179, v4
	v_exp_f32_e32 v178, v8
	v_exp_f32_e32 v181, v12
	v_exp_f32_e32 v180, v16
	v_mfma_f32_32x32x16_bf16 v[18:33], v[118:121], v[166:169], v[18:33]
	v_exp_f32_e32 v2, v2
	v_exp_f32_e32 v6, v6
	v_exp_f32_e32 v10, v10
	v_exp_f32_e32 v12, v14
	v_fma_f32 v4, v179, s12, s12
	v_fma_f32 v8, v178, s12, s12
	v_fma_f32 v14, v181, s12, s12
	v_fma_f32 v16, v180, s12, s12
	v_mfma_f32_32x32x16_bf16 v[18:33], v[114:117], v[162:165], v[18:33]
	v_exp_f32_e32 v3, v3
	v_fmac_f32_e32 v4, v2, v4
	v_exp_f32_e32 v2, v7
	v_fmac_f32_e32 v8, v6, v8
	v_exp_f32_e32 v6, v11
	v_exp_f32_e32 v7, v15
	v_fmac_f32_e32 v14, v10, v14
	v_fmac_f32_e32 v16, v12, v16
	v_mfma_f32_32x32x16_bf16 v[18:33], v[110:113], v[158:161], v[18:33]
	v_add_f32_e32 v10, 1.0, v3
	v_rcp_f32_e32 v3, v4
	v_add_f32_e32 v4, 1.0, v2
	v_rcp_f32_e32 v2, v8
	v_rcp_f32_e32 v183, v14
	v_rcp_f32_e32 v182, v16
	v_mfma_f32_32x32x16_bf16 v[18:33], v[106:109], v[154:157], v[18:33]
	v_add_f32_e32 v6, 1.0, v6
	v_add_f32_e32 v7, 1.0, v7
	v_rcp_f32_e32 v187, v10
	v_rcp_f32_e32 v186, v4
	v_exp_f32_e32 v190, v5
	v_exp_f32_e32 v191, v9
	v_mfma_f32_32x32x16_bf16 v[18:33], v[102:105], v[142:145], v[18:33]
	v_rcp_f32_e32 v189, v6
	v_rcp_f32_e32 v188, v7
	v_exp_f32_e32 v192, v13
	v_exp_f32_e32 v193, v17
	v_mfma_f32_32x32x16_bf16 v[18:33], v[98:101], v[130:133], v[18:33]
	v_fma_f32 v178, -v178, v2, v2
	v_fma_f32 v179, -v179, v3, v3
	v_pk_fma_f32 v[206:207], v[186:187], v[216:217], v[178:179]
	s_nop 0
	v_pk_fma_f32 v[178:179], v[180:181], v[182:183], v[182:183] neg_lo:[1,0,0] neg_hi:[1,0,0]
	s_nop 0
	v_pk_fma_f32 v[208:209], v[188:189], v[218:219], v[178:179]
	s_waitcnt lgkmcnt(0)
	v_mfma_f32_32x32x16_bf16 v[18:33], v[94:97], v[134:137], v[18:33]
	v_add_f32_e32 v178, 1.0, v190
	v_exp_f32_e32 v179, v207
	v_add_f32_e32 v180, 1.0, v191
	v_exp_f32_e32 v181, v206
	v_exp_f32_e32 v182, v209
	v_exp_f32_e32 v183, v208
	v_mfma_f32_32x32x16_bf16 v[18:33], v[90:93], v[138:141], v[18:33]
	v_add_f32_e32 v184, 1.0, v192
	v_add_f32_e32 v185, 1.0, v193
	v_fmac_f32_e32 v178, v178, v179
	v_fmac_f32_e32 v180, v180, v181
	v_fmac_f32_e32 v184, v184, v182
	v_fmac_f32_e32 v185, v185, v183
	v_mfma_f32_32x32x16_bf16 v[18:33], v[86:89], v[146:149], v[18:33]
	v_rcp_f32_e32 v178, v178
	v_rcp_f32_e32 v180, v180
	v_rcp_f32_e32 v184, v184
	v_rcp_f32_e32 v185, v185
	v_mfma_f32_32x32x16_bf16 v[18:33], v[82:85], v[150:153], v[18:33]
	v_fma_f32 v178, -v179, v178, v178
	v_fma_f32 v179, -v181, v180, v180
	v_fma_f32 v180, -v182, v184, v184
	v_fma_f32 v181, -v183, v185, v185
	v_cvt_pk_bf16_f32 v254, v178, v179
	v_cvt_pk_bf16_f32 v255, v180, v181
	ds_write_b128 v211, v[252:255] offset:8192
	s_waitcnt lgkmcnt(0)
	s_barrier
	s_add_i32 s1, s1, 2
	s_cmp_gt_u32 s1, 16
	v_add_u32_e32 v232, 0x200, v232
	s_cbranch_scc1 .LBB1_30
.LBB1_14:
	v_mfma_f32_32x32x16_bf16 v[2:17], v[78:81], v[174:177], v[236:251]
	v_add_u32_e32 v192, v230, v229
	ds_read2_b32 v[228:229], v232 offset1:32
	ds_read_b128 v[194:197], v210 offset:8192
	v_mfma_f32_32x32x16_bf16 v[2:17], v[74:77], v[170:173], v[2:17]
	ds_read_b128 v[178:181], v210 offset:9216
	v_exp_f32_e32 v187, v20
	v_exp_f32_e32 v186, v24
	v_exp_f32_e32 v189, v28
	v_exp_f32_e32 v188, v32
	v_mfma_f32_32x32x16_bf16 v[2:17], v[70:73], v[166:169], v[2:17]
	ds_read_b128 v[170:173], v210 offset:10240
	v_exp_f32_e32 v18, v18
	v_exp_f32_e32 v22, v22
	v_exp_f32_e32 v24, v26
	v_exp_f32_e32 v26, v30
	v_fma_f32 v20, v187, s12, s12
	v_fma_f32 v28, v186, s12, s12
	v_fma_f32 v30, v189, s12, s12
	v_fma_f32 v32, v188, s12, s12
	v_mfma_f32_32x32x16_bf16 v[2:17], v[66:69], v[162:165], v[2:17]
	ds_read_b128 v[166:169], v210 offset:11264
	v_exp_f32_e32 v19, v19
	v_exp_f32_e32 v23, v23
	v_exp_f32_e32 v27, v27
	v_exp_f32_e32 v31, v31
	v_fmac_f32_e32 v20, v18, v20
	v_fmac_f32_e32 v28, v22, v28
	v_fmac_f32_e32 v30, v24, v30
	v_fmac_f32_e32 v32, v26, v32
	v_mfma_f32_32x32x16_bf16 v[2:17], v[62:65], v[158:161], v[2:17]
	ds_read_b128 v[162:165], v210 offset:12288
	v_add_f32_e32 v22, 1.0, v19
	v_rcp_f32_e32 v19, v20
	v_rcp_f32_e32 v18, v28
	v_rcp_f32_e32 v191, v30
	v_rcp_f32_e32 v190, v32
	v_add_f32_e32 v20, 1.0, v23
	v_mfma_f32_32x32x16_bf16 v[2:17], v[58:61], v[154:157], v[2:17]
	ds_read_b128 v[174:177], v210 offset:13312
	v_rcp_f32_e32 v159, v22
	v_rcp_f32_e32 v158, v20
	v_exp_f32_e32 v160, v21
	v_exp_f32_e32 v161, v25
	v_add_f32_e32 v23, 1.0, v27
	v_add_f32_e32 v20, 1.0, v31
	v_mfma_f32_32x32x16_bf16 v[2:17], v[54:57], v[142:145], v[2:17]
	ds_read_b128 v[182:185], v210 offset:14336
	v_rcp_f32_e32 v155, v23
	v_rcp_f32_e32 v154, v20
	v_exp_f32_e32 v193, v29
	v_exp_f32_e32 v217, v33
	v_mfma_f32_32x32x16_bf16 v[2:17], v[50:53], v[130:133], v[2:17]
	ds_read_b128 v[142:145], v210 offset:15360
	v_fma_f32 v156, -v186, v18, v18
	v_fma_f32 v157, -v187, v19, v19
	ds_read_b128 v[18:21], v231 offset:36928
	ds_read_b128 v[22:25], v231 offset:36944
	ds_read_b128 v[26:29], v231 offset:36960
	ds_read_b128 v[30:33], v231 offset:36976
	v_pk_fma_f32 v[214:215], v[158:159], v[214:215], v[156:157]
	v_pk_fma_f32 v[130:131], v[188:189], v[190:191], v[190:191] neg_lo:[1,0,0] neg_hi:[1,0,0]
	s_nop 0
	v_pk_fma_f32 v[212:213], v[154:155], v[212:213], v[130:131]
	v_mfma_f32_32x32x16_bf16 v[2:17], v[46:49], v[134:137], v[2:17]
	ds_read_b128 v[154:157], v192 offset:16384
	v_add_f32_e32 v130, 1.0, v160
	v_exp_f32_e32 v131, v215
	v_exp_f32_e32 v132, v214
	v_exp_f32_e32 v133, v213
	v_exp_f32_e32 v220, v212
	v_add_f32_e32 v134, 1.0, v161
	v_add_f32_e32 v135, 1.0, v193
	v_add_f32_e32 v136, 1.0, v217
	v_mfma_f32_32x32x16_bf16 v[2:17], v[42:45], v[138:141], v[2:17]
	ds_read_b128 v[158:161], v192 offset:16416
	v_fmac_f32_e32 v130, v130, v131
	v_fmac_f32_e32 v134, v134, v132
	v_fmac_f32_e32 v135, v135, v133
	v_fmac_f32_e32 v136, v136, v220
	v_mfma_f32_32x32x16_bf16 v[2:17], v[38:41], v[146:149], v[2:17]
	ds_read_b128 v[186:189], v192 offset:16448
	v_rcp_f32_e32 v130, v130
	v_rcp_f32_e32 v134, v134
	v_mfma_f32_32x32x16_bf16 v[2:17], v[34:37], v[150:153], v[2:17]
	ds_read_b128 v[190:193], v192 offset:16480
	v_rcp_f32_e32 v135, v135
	v_rcp_f32_e32 v136, v136
	v_fma_f32 v130, -v131, v130, v130
	v_fma_f32 v131, -v132, v134, v134
	s_waitcnt lgkmcnt(4)
	v_mfma_f32_32x32x16_bf16 v[18:33], v[126:129], v[194:197], v[18:33]
	v_fma_f32 v132, -v133, v135, v135
	v_fma_f32 v133, -v220, v136, v136
	v_cvt_pk_bf16_f32 v252, v130, v131
	v_cvt_pk_bf16_f32 v253, v132, v133
	v_mfma_f32_32x32x16_bf16 v[18:33], v[122:125], v[178:181], v[18:33]
	s_nop 1
	v_exp_f32_e32 v131, v4
	v_exp_f32_e32 v130, v8
	v_exp_f32_e32 v133, v12
	v_exp_f32_e32 v132, v16
	v_mfma_f32_32x32x16_bf16 v[18:33], v[118:121], v[170:173], v[18:33]
	v_exp_f32_e32 v2, v2
	v_exp_f32_e32 v6, v6
	v_exp_f32_e32 v10, v10
	v_exp_f32_e32 v12, v14
	v_fma_f32 v4, v131, s12, s12
	v_fma_f32 v8, v130, s12, s12
	v_fma_f32 v14, v133, s12, s12
	v_fma_f32 v16, v132, s12, s12
	v_mfma_f32_32x32x16_bf16 v[18:33], v[114:117], v[166:169], v[18:33]
	v_exp_f32_e32 v3, v3
	v_fmac_f32_e32 v4, v2, v4
	v_exp_f32_e32 v2, v7
	v_fmac_f32_e32 v8, v6, v8
	v_exp_f32_e32 v6, v11
	v_exp_f32_e32 v7, v15
	v_fmac_f32_e32 v14, v10, v14
	v_fmac_f32_e32 v16, v12, v16
	v_mfma_f32_32x32x16_bf16 v[18:33], v[110:113], v[162:165], v[18:33]
	v_add_f32_e32 v10, 1.0, v3
	v_rcp_f32_e32 v3, v4
	v_add_f32_e32 v4, 1.0, v2
	v_rcp_f32_e32 v2, v8
	v_rcp_f32_e32 v135, v14
	v_rcp_f32_e32 v134, v16
	v_mfma_f32_32x32x16_bf16 v[18:33], v[106:109], v[174:177], v[18:33]
	v_add_f32_e32 v6, 1.0, v6
	v_add_f32_e32 v7, 1.0, v7
	v_rcp_f32_e32 v137, v10
	v_rcp_f32_e32 v136, v4
	v_exp_f32_e32 v140, v5
	v_exp_f32_e32 v141, v9
	v_mfma_f32_32x32x16_bf16 v[18:33], v[102:105], v[182:185], v[18:33]
	v_rcp_f32_e32 v139, v6
	v_rcp_f32_e32 v138, v7
	v_exp_f32_e32 v146, v13
	v_exp_f32_e32 v147, v17
	v_mfma_f32_32x32x16_bf16 v[18:33], v[98:101], v[142:145], v[18:33]
	v_fma_f32 v130, -v130, v2, v2
	v_fma_f32 v131, -v131, v3, v3
	v_pk_fma_f32 v[224:225], v[136:137], v[204:205], v[130:131]
	s_nop 0
	v_pk_fma_f32 v[130:131], v[132:133], v[134:135], v[134:135] neg_lo:[1,0,0] neg_hi:[1,0,0]
	s_nop 0
	v_pk_fma_f32 v[226:227], v[138:139], v[202:203], v[130:131]
	s_waitcnt lgkmcnt(0)
	v_mfma_f32_32x32x16_bf16 v[18:33], v[94:97], v[154:157], v[18:33]
	v_add_f32_e32 v130, 1.0, v140
	v_exp_f32_e32 v131, v225
	v_add_f32_e32 v132, 1.0, v141
	v_exp_f32_e32 v133, v224
	v_exp_f32_e32 v134, v227
	v_exp_f32_e32 v135, v226
	v_mfma_f32_32x32x16_bf16 v[18:33], v[90:93], v[158:161], v[18:33]
	v_add_f32_e32 v136, 1.0, v146
	v_add_f32_e32 v137, 1.0, v147
	v_fmac_f32_e32 v130, v130, v131
	v_fmac_f32_e32 v132, v132, v133
	v_fmac_f32_e32 v136, v136, v134
	v_fmac_f32_e32 v137, v137, v135
	v_mfma_f32_32x32x16_bf16 v[18:33], v[86:89], v[186:189], v[18:33]
	v_rcp_f32_e32 v130, v130
	v_rcp_f32_e32 v132, v132
	v_rcp_f32_e32 v136, v136
	v_rcp_f32_e32 v137, v137
	v_mfma_f32_32x32x16_bf16 v[18:33], v[82:85], v[190:193], v[18:33]
	v_fma_f32 v130, -v131, v130, v130
	v_fma_f32 v131, -v133, v132, v132
	v_fma_f32 v132, -v134, v136, v136
	v_fma_f32 v133, -v135, v137, v137
	v_cvt_pk_bf16_f32 v254, v130, v131
	v_cvt_pk_bf16_f32 v255, v132, v133
	ds_write_b128 v211, v[252:255] offset:0
	s_waitcnt lgkmcnt(0)
	s_barrier
	v_mfma_f32_32x32x16_bf16 v[2:17], v[78:81], v[194:197], v[236:251]
	ds_read_b128 v[202:205], v210
	v_add_u32_e32 v216, v230, v228
	v_mfma_f32_32x32x16_bf16 v[2:17], v[74:77], v[178:181], v[2:17]
	ds_read_b128 v[194:197], v210 offset:1024
	v_exp_f32_e32 v147, v20
	v_exp_f32_e32 v146, v24
	v_exp_f32_e32 v149, v28
	v_exp_f32_e32 v148, v32
	v_mfma_f32_32x32x16_bf16 v[2:17], v[70:73], v[170:173], v[2:17]
	ds_read_b128 v[138:141], v210 offset:2048
	v_exp_f32_e32 v18, v18
	v_exp_f32_e32 v22, v22
	v_exp_f32_e32 v24, v26
	v_exp_f32_e32 v26, v30
	v_fma_f32 v20, v147, s12, s12
	v_fma_f32 v28, v146, s12, s12
	v_fma_f32 v30, v149, s12, s12
	v_fma_f32 v32, v148, s12, s12
	v_mfma_f32_32x32x16_bf16 v[2:17], v[66:69], v[166:169], v[2:17]
	ds_read_b128 v[134:137], v210 offset:3072
	v_exp_f32_e32 v19, v19
	v_exp_f32_e32 v23, v23
	v_exp_f32_e32 v27, v27
	v_exp_f32_e32 v31, v31
	v_fmac_f32_e32 v20, v18, v20
	v_fmac_f32_e32 v28, v22, v28
	v_fmac_f32_e32 v30, v24, v30
	v_fmac_f32_e32 v32, v26, v32
	v_mfma_f32_32x32x16_bf16 v[2:17], v[62:65], v[162:165], v[2:17]
	ds_read_b128 v[166:169], v210 offset:4096
	v_add_f32_e32 v22, 1.0, v19
	v_rcp_f32_e32 v19, v20
	v_rcp_f32_e32 v18, v28
	v_rcp_f32_e32 v151, v30
	v_rcp_f32_e32 v150, v32
	v_add_f32_e32 v20, 1.0, v23
	v_mfma_f32_32x32x16_bf16 v[2:17], v[58:61], v[174:177], v[2:17]
	ds_read_b128 v[162:165], v210 offset:5120
	v_rcp_f32_e32 v153, v22
	v_rcp_f32_e32 v152, v20
	v_add_f32_e32 v23, 1.0, v27
	v_add_f32_e32 v20, 1.0, v31
	v_exp_f32_e32 v180, v21
	v_exp_f32_e32 v181, v25
	v_mfma_f32_32x32x16_bf16 v[2:17], v[54:57], v[182:185], v[2:17]
	ds_read_b128 v[170:173], v210 offset:6144
	v_rcp_f32_e32 v175, v23
	v_rcp_f32_e32 v174, v20
	v_exp_f32_e32 v176, v29
	v_exp_f32_e32 v177, v33
	v_mfma_f32_32x32x16_bf16 v[2:17], v[50:53], v[142:145], v[2:17]
	ds_read_b128 v[130:133], v210 offset:7168
	v_fma_f32 v146, -v146, v18, v18
	v_fma_f32 v147, -v147, v19, v19
	ds_read_b128 v[18:21], v231 offset:36928
	ds_read_b128 v[22:25], v231 offset:36944
	ds_read_b128 v[26:29], v231 offset:36960
	ds_read_b128 v[30:33], v231 offset:36976
	v_pk_fma_f32 v[220:221], v[152:153], v[200:201], v[146:147]
	v_pk_fma_f32 v[142:143], v[148:149], v[150:151], v[150:151] neg_lo:[1,0,0] neg_hi:[1,0,0]
	s_nop 0
	v_pk_fma_f32 v[222:223], v[174:175], v[198:199], v[142:143]
	v_mfma_f32_32x32x16_bf16 v[2:17], v[46:49], v[154:157], v[2:17]
	ds_read_b128 v[146:149], v216 offset:16384
	v_add_f32_e32 v142, 1.0, v180
	v_exp_f32_e32 v143, v221
	v_exp_f32_e32 v144, v220
	v_exp_f32_e32 v145, v223
	v_exp_f32_e32 v180, v222
	v_add_f32_e32 v154, 1.0, v181
	v_add_f32_e32 v155, 1.0, v176
	v_add_f32_e32 v156, 1.0, v177
	v_mfma_f32_32x32x16_bf16 v[2:17], v[42:45], v[158:161], v[2:17]
	ds_read_b128 v[150:153], v216 offset:16416
	v_fmac_f32_e32 v142, v142, v143
	v_fmac_f32_e32 v154, v154, v144
	v_fmac_f32_e32 v155, v155, v145
	v_fmac_f32_e32 v156, v156, v180
	v_mfma_f32_32x32x16_bf16 v[2:17], v[38:41], v[186:189], v[2:17]
	ds_read_b128 v[174:177], v216 offset:16448
	v_rcp_f32_e32 v142, v142
	v_rcp_f32_e32 v154, v154
	v_mfma_f32_32x32x16_bf16 v[2:17], v[34:37], v[190:193], v[2:17]
	ds_read_b128 v[198:201], v216 offset:16480
	v_rcp_f32_e32 v155, v155
	v_rcp_f32_e32 v156, v156
	v_fma_f32 v142, -v143, v142, v142
	v_fma_f32 v143, -v144, v154, v154
	s_waitcnt lgkmcnt(4)
	v_mfma_f32_32x32x16_bf16 v[18:33], v[126:129], v[202:205], v[18:33]
	v_fma_f32 v144, -v145, v155, v155
	v_fma_f32 v145, -v180, v156, v156
	v_cvt_pk_bf16_f32 v252, v142, v143
	v_cvt_pk_bf16_f32 v253, v144, v145
	v_mfma_f32_32x32x16_bf16 v[18:33], v[122:125], v[194:197], v[18:33]
	s_nop 1
	v_exp_f32_e32 v143, v4
	v_exp_f32_e32 v142, v8
	v_exp_f32_e32 v145, v12
	v_exp_f32_e32 v144, v16
	v_mfma_f32_32x32x16_bf16 v[18:33], v[118:121], v[138:141], v[18:33]
	v_exp_f32_e32 v2, v2
	v_exp_f32_e32 v6, v6
	v_exp_f32_e32 v10, v10
	v_exp_f32_e32 v12, v14
	v_fma_f32 v4, v143, s12, s12
	v_fma_f32 v8, v142, s12, s12
	v_fma_f32 v14, v145, s12, s12
	v_fma_f32 v16, v144, s12, s12
	v_mfma_f32_32x32x16_bf16 v[18:33], v[114:117], v[134:137], v[18:33]
	v_exp_f32_e32 v3, v3
	v_fmac_f32_e32 v4, v2, v4
	v_exp_f32_e32 v2, v7
	v_fmac_f32_e32 v8, v6, v8
	v_exp_f32_e32 v6, v11
	v_exp_f32_e32 v7, v15
	v_fmac_f32_e32 v14, v10, v14
	v_fmac_f32_e32 v16, v12, v16
	v_mfma_f32_32x32x16_bf16 v[18:33], v[110:113], v[166:169], v[18:33]
	v_add_f32_e32 v10, 1.0, v3
	v_rcp_f32_e32 v3, v4
	v_add_f32_e32 v4, 1.0, v2
	v_rcp_f32_e32 v2, v8
	v_rcp_f32_e32 v155, v14
	v_rcp_f32_e32 v154, v16
	v_mfma_f32_32x32x16_bf16 v[18:33], v[106:109], v[162:165], v[18:33]
	v_add_f32_e32 v6, 1.0, v6
	v_add_f32_e32 v7, 1.0, v7
	v_rcp_f32_e32 v157, v10
	v_rcp_f32_e32 v156, v4
	v_exp_f32_e32 v160, v5
	v_exp_f32_e32 v161, v9
	v_mfma_f32_32x32x16_bf16 v[18:33], v[102:105], v[170:173], v[18:33]
	v_rcp_f32_e32 v159, v6
	v_rcp_f32_e32 v158, v7
	v_exp_f32_e32 v180, v13
	v_exp_f32_e32 v181, v17
	v_mfma_f32_32x32x16_bf16 v[18:33], v[98:101], v[130:133], v[18:33]
	v_fma_f32 v142, -v142, v2, v2
	v_fma_f32 v143, -v143, v3, v3
	v_pk_fma_f32 v[216:217], v[156:157], v[206:207], v[142:143]
	s_nop 0
	v_pk_fma_f32 v[142:143], v[144:145], v[154:155], v[154:155] neg_lo:[1,0,0] neg_hi:[1,0,0]
	s_nop 0
	v_pk_fma_f32 v[218:219], v[158:159], v[208:209], v[142:143]
	s_waitcnt lgkmcnt(0)
	v_mfma_f32_32x32x16_bf16 v[18:33], v[94:97], v[146:149], v[18:33]
	v_add_f32_e32 v142, 1.0, v160
	v_exp_f32_e32 v143, v217
	v_add_f32_e32 v144, 1.0, v161
	v_exp_f32_e32 v145, v216
	v_exp_f32_e32 v154, v219
	v_exp_f32_e32 v155, v218
	v_mfma_f32_32x32x16_bf16 v[18:33], v[90:93], v[150:153], v[18:33]
	v_add_f32_e32 v156, 1.0, v180
	v_add_f32_e32 v157, 1.0, v181
	v_fmac_f32_e32 v142, v142, v143
	v_fmac_f32_e32 v144, v144, v145
	v_fmac_f32_e32 v156, v156, v154
	v_fmac_f32_e32 v157, v157, v155
	v_mfma_f32_32x32x16_bf16 v[18:33], v[86:89], v[174:177], v[18:33]
	v_rcp_f32_e32 v142, v142
	v_rcp_f32_e32 v144, v144
	v_rcp_f32_e32 v156, v156
	v_rcp_f32_e32 v157, v157
	v_mfma_f32_32x32x16_bf16 v[18:33], v[82:85], v[198:201], v[18:33]
	v_fma_f32 v142, -v143, v142, v142
	v_fma_f32 v143, -v145, v144, v144
	v_fma_f32 v144, -v154, v156, v156
	v_fma_f32 v145, -v155, v157, v157
	v_cvt_pk_bf16_f32 v254, v142, v143
	v_cvt_pk_bf16_f32 v255, v144, v145
	ds_write_b128 v211, v[252:255] offset:8192
	s_waitcnt lgkmcnt(0)
	s_barrier
	v_mfma_f32_32x32x16_bf16 v[2:17], v[78:81], v[202:205], v[236:251]
	v_add_u32_e32 v234, v230, v229
	ds_read2_b32 v[228:229], v232 offset0:64 offset1:96
	ds_read_b128 v[206:209], v210 offset:8192
	v_mfma_f32_32x32x16_bf16 v[2:17], v[74:77], v[194:197], v[2:17]
	ds_read_b128 v[190:193], v210 offset:9216
	v_exp_f32_e32 v179, v20
	v_exp_f32_e32 v178, v24
	v_exp_f32_e32 v181, v28
	v_exp_f32_e32 v180, v32
	v_mfma_f32_32x32x16_bf16 v[2:17], v[70:73], v[138:141], v[2:17]
	ds_read_b128 v[158:161], v210 offset:10240
	v_exp_f32_e32 v18, v18
	v_exp_f32_e32 v22, v22
	v_exp_f32_e32 v24, v26
	v_exp_f32_e32 v26, v30
	v_fma_f32 v20, v179, s12, s12
	v_fma_f32 v28, v178, s12, s12
	v_fma_f32 v30, v181, s12, s12
	v_fma_f32 v32, v180, s12, s12
	v_mfma_f32_32x32x16_bf16 v[2:17], v[66:69], v[134:137], v[2:17]
	ds_read_b128 v[142:145], v210 offset:11264
	v_exp_f32_e32 v19, v19
	v_exp_f32_e32 v23, v23
	v_exp_f32_e32 v27, v27
	v_exp_f32_e32 v31, v31
	v_fmac_f32_e32 v20, v18, v20
	v_fmac_f32_e32 v28, v22, v28
	v_fmac_f32_e32 v30, v24, v30
	v_fmac_f32_e32 v32, v26, v32
	v_mfma_f32_32x32x16_bf16 v[2:17], v[62:65], v[166:169], v[2:17]
	ds_read_b128 v[154:157], v210 offset:12288
	v_add_f32_e32 v22, 1.0, v19
	v_rcp_f32_e32 v19, v20
	v_rcp_f32_e32 v18, v28
	v_rcp_f32_e32 v139, v30
	v_rcp_f32_e32 v138, v32
	v_add_f32_e32 v20, 1.0, v23
	v_mfma_f32_32x32x16_bf16 v[2:17], v[58:61], v[162:165], v[2:17]
	ds_read_b128 v[182:185], v210 offset:13312
	v_rcp_f32_e32 v141, v22
	v_rcp_f32_e32 v140, v20
	v_add_f32_e32 v23, 1.0, v27
	v_add_f32_e32 v20, 1.0, v31
	v_exp_f32_e32 v168, v21
	v_exp_f32_e32 v169, v25
	v_mfma_f32_32x32x16_bf16 v[2:17], v[54:57], v[170:173], v[2:17]
	ds_read_b128 v[186:189], v210 offset:14336
	v_rcp_f32_e32 v163, v23
	v_rcp_f32_e32 v162, v20
	v_exp_f32_e32 v194, v29
	v_exp_f32_e32 v195, v33
	v_mfma_f32_32x32x16_bf16 v[2:17], v[50:53], v[130:133], v[2:17]
	ds_read_b128 v[134:137], v210 offset:15360
	v_fma_f32 v166, -v178, v18, v18
	v_fma_f32 v167, -v179, v19, v19
	ds_read_b128 v[18:21], v231 offset:36928
	ds_read_b128 v[22:25], v231 offset:36944
	ds_read_b128 v[26:29], v231 offset:36960
	ds_read_b128 v[30:33], v231 offset:36976
	v_pk_fma_f32 v[214:215], v[140:141], v[214:215], v[166:167]
	v_pk_fma_f32 v[130:131], v[180:181], v[138:139], v[138:139] neg_lo:[1,0,0] neg_hi:[1,0,0]
	s_nop 0
	v_pk_fma_f32 v[212:213], v[162:163], v[212:213], v[130:131]
	v_mfma_f32_32x32x16_bf16 v[2:17], v[46:49], v[146:149], v[2:17]
	ds_read_b128 v[138:141], v234 offset:16384
	v_add_f32_e32 v130, 1.0, v168
	v_exp_f32_e32 v131, v215
	v_exp_f32_e32 v132, v214
	v_exp_f32_e32 v133, v213
	v_exp_f32_e32 v162, v212
	v_add_f32_e32 v163, 1.0, v169
	v_add_f32_e32 v166, 1.0, v194
	v_add_f32_e32 v167, 1.0, v195
	v_mfma_f32_32x32x16_bf16 v[2:17], v[42:45], v[150:153], v[2:17]
	ds_read_b128 v[146:149], v234 offset:16416
	v_fmac_f32_e32 v130, v130, v131
	v_fmac_f32_e32 v163, v163, v132
	v_fmac_f32_e32 v166, v166, v133
	v_fmac_f32_e32 v167, v167, v162
	v_mfma_f32_32x32x16_bf16 v[2:17], v[38:41], v[174:177], v[2:17]
	ds_read_b128 v[150:153], v234 offset:16448
	v_rcp_f32_e32 v130, v130
	v_rcp_f32_e32 v163, v163
	v_mfma_f32_32x32x16_bf16 v[2:17], v[34:37], v[198:201], v[2:17]
	ds_read_b128 v[178:181], v234 offset:16480
	v_rcp_f32_e32 v166, v166
	v_rcp_f32_e32 v167, v167
	v_fma_f32 v130, -v131, v130, v130
	v_fma_f32 v131, -v132, v163, v163
	s_waitcnt lgkmcnt(4)
	v_mfma_f32_32x32x16_bf16 v[18:33], v[126:129], v[206:209], v[18:33]
	v_fma_f32 v132, -v133, v166, v166
	v_fma_f32 v133, -v162, v167, v167
	v_cvt_pk_bf16_f32 v252, v130, v131
	v_cvt_pk_bf16_f32 v253, v132, v133
	v_mfma_f32_32x32x16_bf16 v[18:33], v[122:125], v[190:193], v[18:33]
	s_nop 1
	v_exp_f32_e32 v131, v4
	v_exp_f32_e32 v130, v8
	v_exp_f32_e32 v133, v12
	v_exp_f32_e32 v132, v16
	v_mfma_f32_32x32x16_bf16 v[18:33], v[118:121], v[158:161], v[18:33]
	v_exp_f32_e32 v2, v2
	v_exp_f32_e32 v6, v6
	v_exp_f32_e32 v10, v10
	v_exp_f32_e32 v12, v14
	v_fma_f32 v4, v131, s12, s12
	v_fma_f32 v8, v130, s12, s12
	v_fma_f32 v14, v133, s12, s12
	v_fma_f32 v16, v132, s12, s12
	v_mfma_f32_32x32x16_bf16 v[18:33], v[114:117], v[142:145], v[18:33]
	v_exp_f32_e32 v3, v3
	v_fmac_f32_e32 v4, v2, v4
	v_exp_f32_e32 v2, v7
	v_fmac_f32_e32 v8, v6, v8
	v_exp_f32_e32 v6, v11
	v_exp_f32_e32 v7, v15
	v_fmac_f32_e32 v14, v10, v14
	v_fmac_f32_e32 v16, v12, v16
	v_mfma_f32_32x32x16_bf16 v[18:33], v[110:113], v[154:157], v[18:33]
	v_add_f32_e32 v10, 1.0, v3
	v_rcp_f32_e32 v3, v4
	v_add_f32_e32 v4, 1.0, v2
	v_rcp_f32_e32 v2, v8
	v_rcp_f32_e32 v163, v14
	v_rcp_f32_e32 v162, v16
	v_mfma_f32_32x32x16_bf16 v[18:33], v[106:109], v[182:185], v[18:33]
	v_add_f32_e32 v6, 1.0, v6
	v_add_f32_e32 v7, 1.0, v7
	v_rcp_f32_e32 v167, v10
	v_rcp_f32_e32 v166, v4
	v_exp_f32_e32 v170, v5
	v_exp_f32_e32 v171, v9
	v_mfma_f32_32x32x16_bf16 v[18:33], v[102:105], v[186:189], v[18:33]
	v_rcp_f32_e32 v169, v6
	v_rcp_f32_e32 v168, v7
	v_exp_f32_e32 v172, v13
	v_exp_f32_e32 v173, v17
	v_mfma_f32_32x32x16_bf16 v[18:33], v[98:101], v[134:137], v[18:33]
	v_fma_f32 v130, -v130, v2, v2
	v_fma_f32 v131, -v131, v3, v3
	v_pk_fma_f32 v[204:205], v[166:167], v[224:225], v[130:131]
	s_nop 0
	v_pk_fma_f32 v[130:131], v[132:133], v[162:163], v[162:163] neg_lo:[1,0,0] neg_hi:[1,0,0]
	s_nop 0
	v_pk_fma_f32 v[202:203], v[168:169], v[226:227], v[130:131]
	s_waitcnt lgkmcnt(0)
	v_mfma_f32_32x32x16_bf16 v[18:33], v[94:97], v[138:141], v[18:33]
	v_add_f32_e32 v130, 1.0, v170
	v_exp_f32_e32 v131, v205
	v_add_f32_e32 v132, 1.0, v171
	v_exp_f32_e32 v133, v204
	v_exp_f32_e32 v162, v203
	v_exp_f32_e32 v163, v202
	v_mfma_f32_32x32x16_bf16 v[18:33], v[90:93], v[146:149], v[18:33]
	v_add_f32_e32 v164, 1.0, v172
	v_add_f32_e32 v165, 1.0, v173
	v_fmac_f32_e32 v130, v130, v131
	v_fmac_f32_e32 v132, v132, v133
	v_fmac_f32_e32 v164, v164, v162
	v_fmac_f32_e32 v165, v165, v163
	v_mfma_f32_32x32x16_bf16 v[18:33], v[86:89], v[150:153], v[18:33]
	v_rcp_f32_e32 v130, v130
	v_rcp_f32_e32 v132, v132
	v_rcp_f32_e32 v164, v164
	v_rcp_f32_e32 v165, v165
	v_mfma_f32_32x32x16_bf16 v[18:33], v[82:85], v[178:181], v[18:33]
	v_fma_f32 v130, -v131, v130, v130
	v_fma_f32 v131, -v133, v132, v132
	v_fma_f32 v132, -v162, v164, v164
	v_fma_f32 v133, -v163, v165, v165
	v_cvt_pk_bf16_f32 v254, v130, v131
	v_cvt_pk_bf16_f32 v255, v132, v133
	ds_write_b128 v211, v[252:255] offset:0
	s_waitcnt lgkmcnt(0)
	s_barrier
	s_branch .LBB1_13
